# P2: each wave takes 4 consecutive rows instead of rows 2048 apart (page/cache locality); on top of barrier early-invalidate version
# speedup vs baseline: 1.0249x; 1.0249x over previous
; __device__ __forceinline__ void postproj_row(int R, int lane, const bf16* __restrict__ proj, const float* __restrict__ conv_w, const float* __restrict__ g_conv, ...
;     const bf16* pr = proj + (size_t)R * DINP;
;     const bool meta = R >= M; const int b = meta ? 0 : R / S, t = meta ? 0 : R % S, pos = meta ? R - M : t + NMETA;
;     {
;         const u32x2 w = *(const u32x2*)(pr + O_KV + lane * 4);
;         float f[4] = {__uint_as_float(w.x << 16), __uint_as_float(w.x & 0xffff0000u), __uint_as_float(w.y << 16), __uint_as_float(w.y & 0xffff0000u)};
;         const float ss = wave_sum(f[0] * f[0] + f[1] * f[1] + f[2] * f[2] + f[3] * f[3]);
;         const float rstd = rsqrtf(ss * (1.f / KVL) + EPS);
;         const f32x4 g = *(const f32x4*)(g_kv + lane * 4);
;         u32x2 o; o.x = pk2(f[0] * rstd * g.x, f[1] * rstd * g.y); o.y = pk2(f[2] * rstd * g.z, f[3] * rstd * g.w);
;         *(u32x2*)(kvn + (size_t)R * KVL + lane * 4) = o;
;     }
;     if (lane < 32) {
;         const float x1 = bf2f(pr[O_R + lane]), x2 = bf2f(pr[O_R + 32 + lane]);
;         const float cs = cosT[pos * 32 + lane], sn = sinT[pos * 32 + lane];
;         const bf16 o1 = f2bf(x1 * cs - x2 * sn), o2 = f2bf(x1 * sn + x2 * cs);
;         if (!meta) { bf16* d = kpe + (size_t)(b * LP + pos) * ROPE; d[lane] = o1; d[32 + lane] = o2; }
;         else { bf16* d0 = kpe + (size_t)(0 * LP + pos) * ROPE; bf16* d1 = kpe + (size_t)(1 * LP + pos) * ROPE; d0[lane] = o1; d0[32 + lane] = o2; d1[lane] = o1; d1[32 + lane] = o2; }
;     }
;     if (meta) return;
;     {
;         float f[8]; unpack8(*(const u32x4*)(pr + O_Q + lane * 8), f);
;         float ss = 0.f;
; #pragma unroll
;         for (int i = 0; i < 8; ++i) ss += f[i] * f[i];
;         const float rstd = rsqrtf(wave_sum(ss) * (1.f / QL) + EPS);
;         const f32x4 g0 = *(const f32x4*)(g_q + lane * 8), g1 = *(const f32x4*)(g_q + lane * 8 + 4);
;         u32x4 o; o.x = pk2(f[0] * rstd * g0.x, f[1] * rstd * g0.y); o.y = pk2(f[2] * rstd * g0.z, f[3] * rstd * g0.w);
;         o.z = pk2(f[4] * rstd * g1.x, f[5] * rstd * g1.y); o.w = pk2(f[6] * rstd * g1.z, f[7] * rstd * g1.w);
;         *(u32x4*)(qn + (size_t)R * QL + lane * 8) = o;
;     }
;     {
;         const int r1 = (t >= 1) ? R - 1 : M + 15, r2 = (t >= 2) ? R - 2 : (t == 1 ? M + 15 : M + 14);
;         const bf16* p1 = proj + (size_t)r1 * DINP; const bf16* p2 = proj + (size_t)r2 * DINP;
.LBB0_387:
	s_load_dwordx2 s[0:1], s[94:95], 0xb0
	s_waitcnt lgkmcnt(0)
	s_cmp_lt_i32 s0, 3
	s_cselect_b64 s[6:7], -1, 0
	s_and_b64 s[28:29], s[6:7], s[4:5]
	s_andn2_b64 vcc, exec, s[28:29]
	s_cbranch_vccnz .LBB0_400
	s_load_dwordx4 s[8:11], s[94:95], 0x20
	s_load_dwordx2 s[14:15], s[94:95], 0x38
	s_load_dwordx2 s[16:17], s[94:95], 0x48
	s_load_dwordx2 s[36:37], s[94:95], 0xa8
	v_and_b32_e32 v1, 63, v0
	v_readfirstlane_b32 s6, v0
	s_lshl_b32 s7, s2, 3
	s_lshl_b32 s30, s3, 3
	s_lshr_b32 s6, s6, 6
	s_add_i32 s31, s6, s7
	v_lshlrev_b32_e32 v2, 5, v1
	v_lshlrev_b32_e32 v3, 4, v1
	v_lshlrev_b32_e32 v4, 3, v1
	v_lshlrev_b32_e32 v5, 2, v1
	v_lshlrev_b32_e32 v6, 1, v1
	v_lshlrev_b32_e32 v7, 6, v1
	s_waitcnt lgkmcnt(0)
	s_add_u32 s18, s8, 0x1000
	s_addc_u32 s19, s9, 0
	s_add_u32 s20, s8, 0x2000
	s_addc_u32 s21, s9, 0
	global_load_dwordx4 v[8:11], v3, s[14:15]
	global_load_dwordx4 v[12:15], v2, s[10:11]
	global_load_dwordx4 v[16:19], v2, s[10:11] offset:16
	global_load_dwordx4 v[20:23], v7, s[16:17]
	global_load_dwordx4 v[24:27], v7, s[16:17] offset:16
	global_load_dwordx4 v[28:31], v7, s[16:17] offset:32
	global_load_dwordx4 v[32:35], v7, s[16:17] offset:48
	global_load_dwordx4 v[36:39], v7, s[8:9]
	global_load_dwordx4 v[40:43], v7, s[8:9] offset:16
	global_load_dwordx4 v[44:47], v7, s[8:9] offset:32
	global_load_dwordx4 v[48:51], v7, s[8:9] offset:48
	global_load_dwordx4 v[52:55], v7, s[18:19]
	global_load_dwordx4 v[56:59], v7, s[18:19] offset:16
	global_load_dwordx4 v[60:63], v7, s[18:19] offset:32
	global_load_dwordx4 v[64:67], v7, s[18:19] offset:48
	global_load_dwordx4 v[68:71], v7, s[20:21]
	global_load_dwordx4 v[72:75], v7, s[20:21] offset:16
	global_load_dwordx4 v[76:79], v7, s[20:21] offset:32
	global_load_dwordx4 v[80:83], v7, s[20:21] offset:48
	s_add_u32 s44, s36, 0x34000000
	s_addc_u32 s45, s37, 0
	s_add_u32 s46, s36, 0x38200000
	s_addc_u32 s47, s37, 0
	s_add_u32 s34, s36, 0x3a200000
	s_addc_u32 s35, s37, 0
	s_add_u32 s38, s36, 0x3aa00000
	s_addc_u32 s39, s37, 0
	s_add_u32 s40, s36, 0x3b200000
	s_addc_u32 s41, s37, 0
	s_add_u32 s26, s36, 0x41c00000
	s_addc_u32 s27, s37, 0
	s_mov_b32 s19, 1
.Lp2_rpw:
	s_mul_i32 s18, s19, s30
	s_cmpk_lt_u32 s18, 0x2000
	s_cbranch_scc0 .Lp2_rpw_done
	s_add_i32 s19, s19, 1
	s_branch .Lp2_rpw
.Lp2_rpw_done:
	s_mul_i32 s42, s31, s19
	s_add_i32 s19, s42, s19
	s_min_i32 s19, s19, 0x2000
	s_cmp_lt_i32 s42, s19
	s_cbranch_scc0 .Lp2_meta_set
.Lp2_loop:
	s_lshl_b32 s43, s42, 13
	s_add_u32 s48, s44, s43
	s_addc_u32 s49, s45, 0
	s_add_u32 s50, s48, 0x1000
	s_addc_u32 s51, s49, 0
	s_and_b32 s52, s42, 0xfff
	s_lshr_b32 s53, s42, 12
	s_add_i32 s54, s42, -1
	s_cmp_eq_u32 s52, 0
	s_cselect_b32 s54, 0x200f, s54
	s_add_i32 s56, s42, -2
	s_add_i32 s43, s52, 0x200e
	s_cmp_lt_u32 s52, 2
	s_cselect_b32 s56, s43, s56
	s_lshl_b32 s54, s54, 13
	s_lshl_b32 s56, s56, 13
	s_add_u32 s54, s54, 0x800
	s_add_u32 s56, s56, 0x800
	s_add_u32 s54, s44, s54
	s_addc_u32 s55, s45, 0
	s_add_u32 s56, s44, s56
	s_addc_u32 s57, s45, 0
	s_add_i32 s43, s52, 16
	s_lshl_b32 s58, s43, 7
	s_add_u32 s58, s40, s58
	s_addc_u32 s59, s41, 0
	s_add_u32 s4, s58, 0x100000
	s_addc_u32 s5, s59, 0
	global_load_dwordx4 v[108:111], v2, s[54:55]
	global_load_dwordx4 v[112:115], v2, s[54:55] offset:16
	global_load_dwordx4 v[116:119], v2, s[54:55] offset:2048
	global_load_dwordx4 v[120:123], v2, s[54:55] offset:2064
	global_load_dwordx4 v[124:127], v2, s[56:57]
	global_load_dwordx4 v[128:131], v2, s[56:57] offset:16
	global_load_dwordx4 v[132:135], v2, s[56:57] offset:2048
	global_load_dwordx4 v[136:139], v2, s[56:57] offset:2064
	global_load_dwordx4 v[84:87], v2, s[48:49]
	global_load_dwordx4 v[88:91], v2, s[48:49] offset:16
	global_load_dwordx4 v[92:95], v2, s[48:49] offset:2048
	global_load_dwordx4 v[96:99], v2, s[48:49] offset:2064
	global_load_dwordx4 v[100:103], v2, s[50:51]
	global_load_dwordx4 v[104:107], v2, s[50:51] offset:16
	global_load_dwordx4 v[140:143], v3, s[50:51] offset:2048
	global_load_dwordx2 v[144:145], v4, s[50:51] offset:3072
	global_load_ushort v146, v6, s[50:51] offset:3584
	global_load_ushort v147, v6, s[50:51] offset:3648
	global_load_dword v148, v5, s[58:59]
	global_load_dword v149, v5, s[4:5]
	s_lshl_b32 s43, s42, 12
	s_add_u32 s6, s46, s43
	s_addc_u32 s7, s47, 0
	s_lshl_b32 s43, s42, 10
	s_add_u32 s24, s34, s43
	s_addc_u32 s25, s35, 0
	s_lshl_b32 s43, s42, 9
	s_add_u32 s8, s38, s43
	s_addc_u32 s9, s39, 0
	s_mulk_i32 s53, 0x1080
	s_add_i32 s53, s53, s52
	s_add_i32 s53, s53, 16
	s_lshl_b32 s53, s53, 7
	s_add_u32 s10, s26, s53
	s_addc_u32 s11, s27, 0
	v_mov_b32_e32 v206, 0x358637bd
	s_waitcnt vmcnt(0)
; __device__ __forceinline__ void postproj_row(int R, int lane, const bf16* __restrict__ proj, const float* __restrict__ conv_w, const float* __restrict__ g_conv, ...
;     ...
;         const u32x2 w = *(const u32x2*)(pr + O_KV + lane * 4);
;         float f[4] = {__uint_as_float(w.x << 16), __uint_as_float(w.x & 0xffff0000u), __uint_as_float(w.y << 16), __uint_as_float(w.y & 0xffff0000u)};
;         const float ss = wave_sum(f[0] * f[0] + f[1] * f[1] + f[2] * f[2] + f[3] * f[3]);
;         const float rstd = rsqrtf(ss * (1.f / KVL) + EPS);
;         const f32x4 g = *(const f32x4*)(g_kv + lane * 4);
;         u32x2 o; o.x = pk2(f[0] * rstd * g.x, f[1] * rstd * g.y); o.y = pk2(f[2] * rstd * g.z, f[3] * rstd * g.w);
;         *(u32x2*)(kvn + (size_t)R * KVL + lane * 4) = o;
;     }
;     if (lane < 32) {
;         const float x1 = bf2f(pr[O_R + lane]), x2 = bf2f(pr[O_R + 32 + lane]);
;         const float cs = cosT[pos * 32 + lane], sn = sinT[pos * 32 + lane];
;         const bf16 o1 = f2bf(x1 * cs - x2 * sn), o2 = f2bf(x1 * sn + x2 * cs);
;         if (!meta) { bf16* d = kpe + (size_t)(b * LP + pos) * ROPE; d[lane] = o1; d[32 + lane] = o2; }
;         else { bf16* d0 = kpe + (size_t)(0 * LP + pos) * ROPE; bf16* d1 = kpe + (size_t)(1 * LP + pos) * ROPE; d0[lane] = o1; d0[32 + lane] = o2; d1[lane] = o1; d1[32 + lane] = o2; }
;     }
;     if (meta) return;
;     {
;         float f[8]; unpack8(*(const u32x4*)(pr + O_Q + lane * 8), f);
;         float ss = 0.f;
; #pragma unroll
;         for (int i = 0; i < 8; ++i) ss += f[i] * f[i];
;         const float rstd = rsqrtf(wave_sum(ss) * (1.f / QL) + EPS);
;         const f32x4 g0 = *(const f32x4*)(g_q + lane * 8), g1 = *(const f32x4*)(g_q + lane * 8 + 4);
;         u32x4 o; o.x = pk2(f[0] * rstd * g0.x, f[1] * rstd * g0.y); o.y = pk2(f[2] * rstd * g0.z, f[3] * rstd * g0.w);
;         o.z = pk2(f[4] * rstd * g1.x, f[5] * rstd * g1.y); o.w = pk2(f[6] * rstd * g1.z, f[7] * rstd * g1.w);
;         *(u32x4*)(qn + (size_t)R * QL + lane * 8) = o;
;     }
;     {
;         const int r1 = (t >= 1) ? R - 1 : M + 15, r2 = (t >= 2) ? R - 2 : (t == 1 ? M + 15 : M + 14);
;         const bf16* p1 = proj + (size_t)r1 * DINP; const bf16* p2 = proj + (size_t)r2 * DINP;
;         const int c0 = lane * 16;
;         float v[16]; float ss = 0.f;
; #pragma unroll
;         for (int hh = 0; hh < 2; ++hh) {
	v_lshlrev_b32_e32 v186, 16, v140
	v_and_b32_e32 v187, 0xffff0000, v140
	v_lshlrev_b32_e32 v188, 16, v141
	v_and_b32_e32 v189, 0xffff0000, v141
	v_lshlrev_b32_e32 v190, 16, v142
	v_and_b32_e32 v191, 0xffff0000, v142
	v_lshlrev_b32_e32 v192, 16, v143
	v_and_b32_e32 v193, 0xffff0000, v143
	v_mul_f32_e32 v194, v186, v186
	v_fmac_f32_e32 v194, v187, v187
	v_fmac_f32_e32 v194, v188, v188
	v_fmac_f32_e32 v194, v189, v189
	v_fmac_f32_e32 v194, v190, v190
	v_fmac_f32_e32 v194, v191, v191
	v_fmac_f32_e32 v194, v192, v192
	v_fmac_f32_e32 v194, v193, v193
	v_lshlrev_b32_e32 v196, 16, v144
	v_and_b32_e32 v197, 0xffff0000, v144
	v_lshlrev_b32_e32 v198, 16, v145
	v_and_b32_e32 v199, 0xffff0000, v145
	v_mul_f32_e32 v195, v196, v196
	v_fmac_f32_e32 v195, v197, v197
	v_fmac_f32_e32 v195, v198, v198
	v_fmac_f32_e32 v195, v199, v199
	s_nop 1
	v_add_f32_dpp v194, v194, v194 quad_perm:[1,0,3,2] row_mask:0xf bank_mask:0xf
	v_add_f32_dpp v195, v195, v195 quad_perm:[1,0,3,2] row_mask:0xf bank_mask:0xf
	s_nop 1
	v_add_f32_dpp v194, v194, v194 quad_perm:[2,3,0,1] row_mask:0xf bank_mask:0xf
	v_add_f32_dpp v195, v195, v195 quad_perm:[2,3,0,1] row_mask:0xf bank_mask:0xf
	s_nop 1
	v_add_f32_dpp v194, v194, v194 row_half_mirror row_mask:0xf bank_mask:0xf
	v_add_f32_dpp v195, v195, v195 row_half_mirror row_mask:0xf bank_mask:0xf
	s_nop 1
	v_add_f32_dpp v194, v194, v194 row_mirror row_mask:0xf bank_mask:0xf
	v_add_f32_dpp v195, v195, v195 row_mirror row_mask:0xf bank_mask:0xf
	s_nop 1
	v_add_f32_dpp v194, v194, v194 row_bcast:15 row_mask:0xa bank_mask:0xf
	v_add_f32_dpp v195, v195, v195 row_bcast:15 row_mask:0xa bank_mask:0xf
	s_nop 1
	v_add_f32_dpp v194, v194, v194 row_bcast:31 row_mask:0xc bank_mask:0xf
	v_add_f32_dpp v195, v195, v195 row_bcast:31 row_mask:0xc bank_mask:0xf
	v_lshlrev_b32_e32 v150, 16, v92
	v_and_b32_e32 v151, 0xffff0000, v92
	v_lshlrev_b32_e32 v152, 16, v100
	v_and_b32_e32 v153, 0xffff0000, v100
	v_pk_mul_f32 v[150:151], v[150:151], v[152:153]
	v_lshlrev_b32_e32 v152, 16, v108
	v_and_b32_e32 v153, 0xffff0000, v108
	v_lshlrev_b32_e32 v154, 16, v116
	v_and_b32_e32 v155, 0xffff0000, v116
	v_pk_mul_f32 v[152:153], v[152:153], v[154:155]
	v_lshlrev_b32_e32 v154, 16, v124
	v_and_b32_e32 v155, 0xffff0000, v124
	v_lshlrev_b32_e32 v156, 16, v132
	v_and_b32_e32 v157, 0xffff0000, v132
	v_pk_mul_f32 v[154:155], v[154:155], v[156:157]
	v_pk_mul_f32 v[152:153], v[52:53], v[152:153]
	v_pk_fma_f32 v[152:153], v[68:69], v[150:151], v[152:153]
	v_pk_fma_f32 v[152:153], v[36:37], v[154:155], v[152:153]
	v_lshlrev_b32_e32 v156, 16, v84
	v_and_b32_e32 v157, 0xffff0000, v84
	v_pk_mul_f32 v[160:161], v[156:157], v[152:153]
	v_mul_f32_e32 v158, v160, v160
	v_fmac_f32_e32 v158, v161, v161
	v_lshlrev_b32_e32 v150, 16, v93
	v_and_b32_e32 v151, 0xffff0000, v93
	v_lshlrev_b32_e32 v152, 16, v101
	v_and_b32_e32 v153, 0xffff0000, v101
	v_pk_mul_f32 v[150:151], v[150:151], v[152:153]
	v_lshlrev_b32_e32 v152, 16, v109
	v_and_b32_e32 v153, 0xffff0000, v109
	v_lshlrev_b32_e32 v154, 16, v117
	v_and_b32_e32 v155, 0xffff0000, v117
	v_pk_mul_f32 v[152:153], v[152:153], v[154:155]
	v_lshlrev_b32_e32 v154, 16, v125
	v_and_b32_e32 v155, 0xffff0000, v125
	v_lshlrev_b32_e32 v156, 16, v133
	v_and_b32_e32 v157, 0xffff0000, v133
	v_pk_mul_f32 v[154:155], v[154:155], v[156:157]
	v_pk_mul_f32 v[152:153], v[54:55], v[152:153]
	v_pk_fma_f32 v[152:153], v[70:71], v[150:151], v[152:153]
	v_pk_fma_f32 v[152:153], v[38:39], v[154:155], v[152:153]
	v_lshlrev_b32_e32 v156, 16, v85
	v_and_b32_e32 v157, 0xffff0000, v85
	v_pk_mul_f32 v[162:163], v[156:157], v[152:153]
	v_fmac_f32_e32 v158, v162, v162
	v_fmac_f32_e32 v158, v163, v163
	v_lshlrev_b32_e32 v150, 16, v94
	v_and_b32_e32 v151, 0xffff0000, v94
	v_lshlrev_b32_e32 v152, 16, v102
	v_and_b32_e32 v153, 0xffff0000, v102
	v_pk_mul_f32 v[150:151], v[150:151], v[152:153]
	v_lshlrev_b32_e32 v152, 16, v110
	v_and_b32_e32 v153, 0xffff0000, v110
	v_lshlrev_b32_e32 v154, 16, v118
	v_and_b32_e32 v155, 0xffff0000, v118
	v_pk_mul_f32 v[152:153], v[152:153], v[154:155]
	v_lshlrev_b32_e32 v154, 16, v126
	v_and_b32_e32 v155, 0xffff0000, v126
	v_lshlrev_b32_e32 v156, 16, v134
	v_and_b32_e32 v157, 0xffff0000, v134
	v_pk_mul_f32 v[154:155], v[154:155], v[156:157]
	v_pk_mul_f32 v[152:153], v[56:57], v[152:153]
	v_pk_fma_f32 v[152:153], v[72:73], v[150:151], v[152:153]
	v_pk_fma_f32 v[152:153], v[40:41], v[154:155], v[152:153]
	v_lshlrev_b32_e32 v156, 16, v86
	v_and_b32_e32 v157, 0xffff0000, v86
	v_pk_mul_f32 v[164:165], v[156:157], v[152:153]
	v_fmac_f32_e32 v158, v164, v164
	v_fmac_f32_e32 v158, v165, v165
	v_lshlrev_b32_e32 v150, 16, v95
	v_and_b32_e32 v151, 0xffff0000, v95
	v_lshlrev_b32_e32 v152, 16, v103
	v_and_b32_e32 v153, 0xffff0000, v103
	v_pk_mul_f32 v[150:151], v[150:151], v[152:153]
	v_lshlrev_b32_e32 v152, 16, v111
	v_and_b32_e32 v153, 0xffff0000, v111
	v_lshlrev_b32_e32 v154, 16, v119
	v_and_b32_e32 v155, 0xffff0000, v119
	v_pk_mul_f32 v[152:153], v[152:153], v[154:155]
	v_lshlrev_b32_e32 v154, 16, v127
	v_and_b32_e32 v155, 0xffff0000, v127
	v_lshlrev_b32_e32 v156, 16, v135
	v_and_b32_e32 v157, 0xffff0000, v135
	v_pk_mul_f32 v[154:155], v[154:155], v[156:157]
	v_pk_mul_f32 v[152:153], v[58:59], v[152:153]
	v_pk_fma_f32 v[152:153], v[74:75], v[150:151], v[152:153]
	v_pk_fma_f32 v[152:153], v[42:43], v[154:155], v[152:153]
	v_lshlrev_b32_e32 v156, 16, v87
	v_and_b32_e32 v157, 0xffff0000, v87
	v_pk_mul_f32 v[166:167], v[156:157], v[152:153]
	v_fmac_f32_e32 v158, v166, v166
	v_fmac_f32_e32 v158, v167, v167
	v_lshlrev_b32_e32 v150, 16, v96
	v_and_b32_e32 v151, 0xffff0000, v96
	v_lshlrev_b32_e32 v152, 16, v104
	v_and_b32_e32 v153, 0xffff0000, v104
; __device__ __forceinline__ float bf2f(bf16 v) { return __uint_as_float((unsigned)v << 16); }
; __device__ __forceinline__ void postproj_row(int R, int lane, const bf16* __restrict__ proj, const float* __restrict__ conv_w, const float* __restrict__ g_conv, ...
;     ...
;         const float x1 = bf2f(pr[O_R + lane]), x2 = bf2f(pr[O_R + 32 + lane]);
;         const float cs = cosT[pos * 32 + lane], sn = sinT[pos * 32 + lane];
;         const bf16 o1 = f2bf(x1 * cs - x2 * sn), o2 = f2bf(x1 * sn + x2 * cs);
;         if (!meta) { bf16* d = kpe + (size_t)(b * LP + pos) * ROPE; d[lane] = o1; d[32 + lane] = o2; }
;         else { bf16* d0 = kpe + (size_t)(0 * LP + pos) * ROPE; bf16* d1 = kpe + (size_t)(1 * LP + pos) * ROPE; d0[lane] = o1; d0[32 + lane] = o2; d1[lane] = o1; d1[32 + lane] = o2; }
;     }
;     if (meta) return;
;     {
;         float f[8]; unpack8(*(const u32x4*)(pr + O_Q + lane * 8), f);
;         float ss = 0.f;
; #pragma unroll
;         for (int i = 0; i < 8; ++i) ss += f[i] * f[i];
;         const float rstd = rsqrtf(wave_sum(ss) * (1.f / QL) + EPS);
;         const f32x4 g0 = *(const f32x4*)(g_q + lane * 8), g1 = *(const f32x4*)(g_q + lane * 8 + 4);
;         u32x4 o; o.x = pk2(f[0] * rstd * g0.x, f[1] * rstd * g0.y); o.y = pk2(f[2] * rstd * g0.z, f[3] * rstd * g0.w);
;         o.z = pk2(f[4] * rstd * g1.x, f[5] * rstd * g1.y); o.w = pk2(f[6] * rstd * g1.z, f[7] * rstd * g1.w);
;         *(u32x4*)(qn + (size_t)R * QL + lane * 8) = o;
;     }
;     {
;         const int r1 = (t >= 1) ? R - 1 : M + 15, r2 = (t >= 2) ? R - 2 : (t == 1 ? M + 15 : M + 14);
;         const bf16* p1 = proj + (size_t)r1 * DINP; const bf16* p2 = proj + (size_t)r2 * DINP;
;         const int c0 = lane * 16;
;         float v[16]; float ss = 0.f;
; #pragma unroll
;         for (int hh = 0; hh < 2; ++hh) {
;             const int c = c0 + hh * 8;
;             float bg[8], cg0[8], ui0[8], cg1[8], ui1[8], cg2[8], ui2[8];
;             unpack8(*(const u32x4*)(pr + c), bg); unpack8(*(const u32x4*)(pr + O_C + c), cg0); unpack8(*(const u32x4*)(pr + O_U + c), ui0);
;             unpack8(*(const u32x4*)(p1 + O_C + c), cg1); unpack8(*(const u32x4*)(p1 + O_U + c), ui1);
;             unpack8(*(const u32x4*)(p2 + O_C + c), cg2); unpack8(*(const u32x4*)(p2 + O_U + c), ui2);
; #pragma unroll
;             for (int i = 0; i < 8; ++i) {
	v_pk_mul_f32 v[150:151], v[150:151], v[152:153]
	v_lshlrev_b32_e32 v152, 16, v112
	v_and_b32_e32 v153, 0xffff0000, v112
	v_lshlrev_b32_e32 v154, 16, v120
	v_and_b32_e32 v155, 0xffff0000, v120
	v_pk_mul_f32 v[152:153], v[152:153], v[154:155]
	v_lshlrev_b32_e32 v154, 16, v128
	v_and_b32_e32 v155, 0xffff0000, v128
	v_lshlrev_b32_e32 v156, 16, v136
	v_and_b32_e32 v157, 0xffff0000, v136
	v_pk_mul_f32 v[154:155], v[154:155], v[156:157]
	v_pk_mul_f32 v[152:153], v[60:61], v[152:153]
	v_pk_fma_f32 v[152:153], v[76:77], v[150:151], v[152:153]
	v_pk_fma_f32 v[152:153], v[44:45], v[154:155], v[152:153]
	v_lshlrev_b32_e32 v156, 16, v88
	v_and_b32_e32 v157, 0xffff0000, v88
	v_pk_mul_f32 v[168:169], v[156:157], v[152:153]
	v_fmac_f32_e32 v158, v168, v168
	v_fmac_f32_e32 v158, v169, v169
	v_lshlrev_b32_e32 v150, 16, v97
	v_and_b32_e32 v151, 0xffff0000, v97
	v_lshlrev_b32_e32 v152, 16, v105
	v_and_b32_e32 v153, 0xffff0000, v105
	v_pk_mul_f32 v[150:151], v[150:151], v[152:153]
	v_lshlrev_b32_e32 v152, 16, v113
	v_and_b32_e32 v153, 0xffff0000, v113
	v_lshlrev_b32_e32 v154, 16, v121
	v_and_b32_e32 v155, 0xffff0000, v121
	v_pk_mul_f32 v[152:153], v[152:153], v[154:155]
	v_lshlrev_b32_e32 v154, 16, v129
	v_and_b32_e32 v155, 0xffff0000, v129
	v_lshlrev_b32_e32 v156, 16, v137
	v_and_b32_e32 v157, 0xffff0000, v137
	v_pk_mul_f32 v[154:155], v[154:155], v[156:157]
	v_pk_mul_f32 v[152:153], v[62:63], v[152:153]
	v_pk_fma_f32 v[152:153], v[78:79], v[150:151], v[152:153]
	v_pk_fma_f32 v[152:153], v[46:47], v[154:155], v[152:153]
	v_lshlrev_b32_e32 v156, 16, v89
	v_and_b32_e32 v157, 0xffff0000, v89
	v_pk_mul_f32 v[170:171], v[156:157], v[152:153]
	v_fmac_f32_e32 v158, v170, v170
	v_fmac_f32_e32 v158, v171, v171
	v_lshlrev_b32_e32 v150, 16, v98
	v_and_b32_e32 v151, 0xffff0000, v98
	v_lshlrev_b32_e32 v152, 16, v106
	v_and_b32_e32 v153, 0xffff0000, v106
	v_pk_mul_f32 v[150:151], v[150:151], v[152:153]
	v_lshlrev_b32_e32 v152, 16, v114
	v_and_b32_e32 v153, 0xffff0000, v114
	v_lshlrev_b32_e32 v154, 16, v122
	v_and_b32_e32 v155, 0xffff0000, v122
	v_pk_mul_f32 v[152:153], v[152:153], v[154:155]
	v_lshlrev_b32_e32 v154, 16, v130
	v_and_b32_e32 v155, 0xffff0000, v130
	v_lshlrev_b32_e32 v156, 16, v138
	v_and_b32_e32 v157, 0xffff0000, v138
	v_pk_mul_f32 v[154:155], v[154:155], v[156:157]
	v_pk_mul_f32 v[152:153], v[64:65], v[152:153]
	v_pk_fma_f32 v[152:153], v[80:81], v[150:151], v[152:153]
	v_pk_fma_f32 v[152:153], v[48:49], v[154:155], v[152:153]
	v_lshlrev_b32_e32 v156, 16, v90
	v_and_b32_e32 v157, 0xffff0000, v90
	v_pk_mul_f32 v[172:173], v[156:157], v[152:153]
	v_fmac_f32_e32 v158, v172, v172
	v_fmac_f32_e32 v158, v173, v173
	v_lshlrev_b32_e32 v150, 16, v99
	v_and_b32_e32 v151, 0xffff0000, v99
	v_lshlrev_b32_e32 v152, 16, v107
	v_and_b32_e32 v153, 0xffff0000, v107
	v_pk_mul_f32 v[150:151], v[150:151], v[152:153]
	v_lshlrev_b32_e32 v152, 16, v115
	v_and_b32_e32 v153, 0xffff0000, v115
	v_lshlrev_b32_e32 v154, 16, v123
	v_and_b32_e32 v155, 0xffff0000, v123
	v_pk_mul_f32 v[152:153], v[152:153], v[154:155]
	v_lshlrev_b32_e32 v154, 16, v131
	v_and_b32_e32 v155, 0xffff0000, v131
	v_lshlrev_b32_e32 v156, 16, v139
	v_and_b32_e32 v157, 0xffff0000, v139
	v_pk_mul_f32 v[154:155], v[154:155], v[156:157]
	v_pk_mul_f32 v[152:153], v[66:67], v[152:153]
	v_pk_fma_f32 v[152:153], v[82:83], v[150:151], v[152:153]
	v_pk_fma_f32 v[152:153], v[50:51], v[154:155], v[152:153]
	v_lshlrev_b32_e32 v156, 16, v91
	v_and_b32_e32 v157, 0xffff0000, v91
	v_pk_mul_f32 v[174:175], v[156:157], v[152:153]
	v_fmac_f32_e32 v158, v174, v174
	v_fmac_f32_e32 v158, v175, v175
	v_readlane_b32 s43, v194, 63
	v_readlane_b32 s53, v195, 63
	s_nop 0
	v_add_f32_dpp v158, v158, v158 quad_perm:[1,0,3,2] row_mask:0xf bank_mask:0xf
	v_mov_b32_e32 v151, s43
	v_mov_b32_e32 v152, s53
	v_add_f32_dpp v158, v158, v158 quad_perm:[2,3,0,1] row_mask:0xf bank_mask:0xf
	v_fmamk_f32 v151, v151, 0x3b000000, v206
	v_fmamk_f32 v152, v152, 0x3b800000, v206
	v_fmamk_f32 v158, v158, 0x3c800000, v206
	v_rsq_f32_e32 v151, v151
	v_rsq_f32_e32 v152, v152
	v_rsq_f32_e32 v158, v158
	s_nop 0
	v_mov_b32_e32 v159, v158
	v_mul_f32_e32 v186, v151, v186
	v_mul_f32_e32 v187, v151, v187
	v_mul_f32_e32 v188, v151, v188
	v_mul_f32_e32 v189, v151, v189
	v_mul_f32_e32 v190, v151, v190
	v_mul_f32_e32 v191, v151, v191
	v_mul_f32_e32 v192, v151, v192
	v_mul_f32_e32 v193, v151, v193
	v_mul_f32_e32 v186, v12, v186
	v_mul_f32_e32 v187, v13, v187
	v_mul_f32_e32 v188, v14, v188
	v_mul_f32_e32 v189, v15, v189
	v_mul_f32_e32 v190, v16, v190
	v_mul_f32_e32 v191, v17, v191
	v_mul_f32_e32 v192, v18, v192
	v_mul_f32_e32 v193, v19, v193
	v_cvt_pk_bf16_f32 v200, v186, v187
	v_cvt_pk_bf16_f32 v201, v188, v189
	v_cvt_pk_bf16_f32 v202, v190, v191
	v_cvt_pk_bf16_f32 v203, v192, v193
	global_store_dwordx4 v3, v[200:203], s[24:25]
	v_mul_f32_e32 v196, v152, v196
	v_mul_f32_e32 v197, v152, v197
	v_mul_f32_e32 v198, v152, v198
	v_mul_f32_e32 v199, v152, v199
	v_mul_f32_e32 v196, v8, v196
	v_mul_f32_e32 v197, v9, v197
	v_mul_f32_e32 v198, v10, v198
	v_mul_f32_e32 v199, v11, v199
	v_cvt_pk_bf16_f32 v204, v196, v197
	v_cvt_pk_bf16_f32 v205, v198, v199
	global_store_dwordx2 v4, v[204:205], s[8:9]
	v_pk_mul_f32 v[160:161], v[160:161], v[158:159]
	v_pk_mul_f32 v[162:163], v[162:163], v[158:159]
	v_pk_mul_f32 v[164:165], v[164:165], v[158:159]
	v_pk_mul_f32 v[166:167], v[166:167], v[158:159]
	v_pk_mul_f32 v[168:169], v[168:169], v[158:159]
	v_pk_mul_f32 v[170:171], v[170:171], v[158:159]
	v_pk_mul_f32 v[172:173], v[172:173], v[158:159]
	v_pk_mul_f32 v[174:175], v[174:175], v[158:159]
	v_pk_mul_f32 v[160:161], v[160:161], v[20:21]
	v_pk_mul_f32 v[162:163], v[162:163], v[22:23]
	v_pk_mul_f32 v[164:165], v[164:165], v[24:25]
	v_pk_mul_f32 v[166:167], v[166:167], v[26:27]
	v_pk_mul_f32 v[168:169], v[168:169], v[28:29]
	v_pk_mul_f32 v[170:171], v[170:171], v[30:31]
	v_pk_mul_f32 v[172:173], v[172:173], v[32:33]
	v_pk_mul_f32 v[174:175], v[174:175], v[34:35]
	v_cvt_pk_bf16_f32 v178, v160, v161
	v_cvt_pk_bf16_f32 v179, v162, v163
	v_cvt_pk_bf16_f32 v180, v164, v165
	v_cvt_pk_bf16_f32 v181, v166, v167
	v_cvt_pk_bf16_f32 v182, v168, v169
	v_cvt_pk_bf16_f32 v183, v170, v171
	v_cvt_pk_bf16_f32 v184, v172, v173
	v_cvt_pk_bf16_f32 v185, v174, v175
	global_store_dwordx4 v2, v[178:181], s[6:7]
	global_store_dwordx4 v2, v[182:185], s[6:7] offset:16
	v_lshlrev_b32_e32 v146, 16, v146
	v_lshlrev_b32_e32 v147, 16, v147
	v_mul_f32_e32 v153, v149, v147
	v_mul_f32_e32 v154, v148, v147
	v_fma_f32 v153, v148, v146, -v153
	v_fmac_f32_e32 v154, v149, v146
	v_cvt_pk_bf16_f32 v155, v153, v154
	s_mov_b32 exec_hi, 0
	global_store_short v6, v155, s[10:11]
	global_store_short_d16_hi v6, v155, s[10:11] offset:64
	s_mov_b32 exec_hi, -1
	s_add_i32 s42, s42, 1
	s_cmp_lt_i32 s42, s19
	s_cbranch_scc1 .Lp2_loop
.Lp2_meta_set:
	s_add_i32 s42, s31, 0x2000
